# combo16 + phase 2 V-transpose thread map changed so each transposed store instruction fills whole 128-byte lines
# speedup vs baseline: 1.0153x; 1.0153x over previous
.LBB0_432:
	s_cmp_lt_i32 s48, 3
	s_cselect_b64 s[6:7], -1, 0
	s_and_b64 s[56:57], s[6:7], s[4:5]
	s_andn2_b64 vcc, exec, s[56:57]
	s_cbranch_vccnz .LBB0_453
	s_cmpk_gt_i32 s2, 0xff
	s_cbranch_scc1 .LBB0_453
	s_load_dwordx2 s[58:59], s[0:1], 0xb0
	s_load_dwordx2 s[84:85], s[0:1], 0x18
	s_load_dwordx4 s[44:47], s[0:1], 0x38
	s_waitcnt vmcnt(7)
	v_lshlrev_b32_e32 v2, 3, v0
	v_writelane_b32 v246, s92, 0
	v_and_b32_e32 v122, 63, v0
	s_waitcnt lgkmcnt(0)
	s_add_u32 s60, s58, 0x42c4a000
	s_addc_u32 s61, s59, 0
	s_add_u32 s62, s58, 0x39c4a000
	s_addc_u32 s63, s59, 0
	s_add_u32 s64, s58, 0x3bc4a000
	s_addc_u32 s65, s59, 0
	s_add_u32 s66, s58, 0x3dc4a000
	s_addc_u32 s67, s59, 0
	s_add_u32 s68, s58, 0x3e44a000
	s_addc_u32 s69, s59, 0
	s_add_u32 s72, s58, 0x10000
	s_addc_u32 s73, s59, 0
	s_add_u32 s74, s58, 0x50000
	s_addc_u32 s75, s59, 0
	s_add_u32 s76, s58, 0x90000
	s_addc_u32 s77, s59, 0
	s_add_u32 s78, s58, 0xd0000
	s_addc_u32 s79, s59, 0
	s_add_u32 s80, s58, 0x110000
	s_addc_u32 s81, s59, 0
	v_writelane_b32 v246, s93, 1
	v_lshrrev_b32_e32 v1, 6, v0
	v_and_b32_e32 v2, 0x3f8, v2
	v_lshrrev_b32_e32 v3, 3, v0
	v_mov_b32_e32 v127, 0
	s_movk_i32 s92, 0x100
	s_add_u32 s82, s58, 0x42c4c000
	v_and_b32_e32 v124, 56, v0
	v_cmp_gt_u32_e64 s[4:5], s92, v0
	s_mov_b32 s71, 0
	v_cmp_eq_u32_e64 s[6:7], 0, v122
	v_cmp_gt_u32_e64 s[8:9], 2, v122
	v_cmp_gt_u32_e64 s[10:11], 4, v122
	v_cmp_gt_u32_e64 s[12:13], 8, v122
	v_cmp_gt_u32_e64 s[14:15], 16, v122
	v_cmp_gt_u32_e64 s[16:17], 32, v122
	v_lshlrev_b32_e32 v123, 3, v1
	v_and_b32_e32 v128, 56, v3
	v_mov_b32_e32 v129, v127
	s_addc_u32 s83, s59, 0
	s_movk_i32 s93, 0x4c00
	v_mov_b64_e32 v[130:131], s[60:61]
	v_mov_b32_e32 v125, 0x4c00
	v_and_b32_e32 v132, 7, v0
	v_lshlrev_b32_e32 v132, 4, v132
	v_lshrrev_b32_e32 v2, 6, v0
	v_lshl_add_u32 v132, v2, 8, v132
	v_mov_b32_e32 v133, v127
	s_mov_b32 s94, 0xffff
	s_mov_b32 s95, 0xffff0000
	s_movk_i32 s96, 0x2000
	s_movk_i32 s97, 0x4000
	s_movk_i32 s54, 0x6000
	s_mov_b32 s55, 0xc2fc0000
	v_mov_b32_e32 v212, 0x358637bd
	s_mov_b32 s52, 0x800000
	v_mbcnt_lo_u32_b32 v213, -1, 0
	v_mov_b32_e32 v214, 0x33c4a000
	v_mov_b32_e32 v215, 0x35c4a000
	v_mov_b32_e32 v216, 0x42800000
	v_not_b32_e32 v217, 63
	v_mov_b32_e32 v218, 0xffffff60
	s_mov_b32 s53, s2
	s_mov_b64 s[86:87], 0x9800
	s_mov_b32 s88, s2
	s_branch .LBB0_436

.LBB0_436:
	s_ashr_i32 s89, s88, 31
	s_lshl_b64 s[42:43], s[88:89], 6
	v_or_b32_e32 v34, s42, v124
	v_mad_u64_u32 v[34:35], s[18:19], v34, s93, v[130:131]
	v_mad_i32_i24 v35, s43, v125, v35
	v_lshl_add_u64 v[58:59], v[34:35], 0, v[132:133]
	s_movk_i32 s18, 0x1000
	v_add_co_u32_e32 v34, vcc, s18, v58
	s_movk_i32 s18, 0x5000
	s_nop 0
	v_addc_co_u32_e32 v35, vcc, 0, v59, vcc
	v_add_co_u32_e32 v36, vcc, s18, v58
	s_mov_b32 s18, 0xa000
	s_nop 0
	v_addc_co_u32_e32 v37, vcc, 0, v59, vcc
	global_load_dwordx4 v[66:69], v[34:35], off
	global_load_dwordx4 v[70:73], v[36:37], off offset:3072
	v_add_co_u32_e32 v34, vcc, s18, v58
	s_mov_b32 s18, 0xf000
	s_nop 0
	v_addc_co_u32_e32 v35, vcc, 0, v59, vcc
	v_add_co_u32_e32 v36, vcc, s18, v58
	s_mov_b32 s18, 0x14000
	s_nop 0
	v_addc_co_u32_e32 v37, vcc, 0, v59, vcc
	global_load_dwordx4 v[74:77], v[34:35], off offset:2048
	global_load_dwordx4 v[78:81], v[36:37], off offset:1024
	v_add_co_u32_e32 v34, vcc, s18, v58
	s_mov_b32 s18, 0x18000
	s_nop 0
	v_addc_co_u32_e32 v35, vcc, 0, v59, vcc
	v_add_co_u32_e32 v36, vcc, s18, v58
	s_mov_b32 s18, 0x1d000
	s_nop 0
	v_addc_co_u32_e32 v37, vcc, 0, v59, vcc
	global_load_dwordx4 v[82:85], v[34:35], off
	global_load_dwordx4 v[86:89], v[36:37], off offset:3072
	v_add_co_u32_e32 v34, vcc, s18, v58
	s_mov_b32 s18, 0x22000
	s_nop 0
	v_addc_co_u32_e32 v35, vcc, 0, v59, vcc
	v_add_co_u32_e32 v36, vcc, s18, v58
	s_mov_b32 s18, 0x1000
	s_nop 0
	v_addc_co_u32_e32 v37, vcc, 0, v59, vcc
	global_load_dwordx4 v[90:93], v[34:35], off offset:2048
	global_load_dwordx4 v[94:97], v[36:37], off offset:1024
	v_add_co_u32_e32 v34, vcc, s18, v58
	s_mov_b32 s18, 0x5000
	s_nop 0
	v_addc_co_u32_e32 v35, vcc, 0, v59, vcc
	v_add_co_u32_e32 v38, vcc, s18, v58
	s_mov_b32 s18, 0xa000
	s_nop 0
	v_addc_co_u32_e32 v39, vcc, 0, v59, vcc
	v_add_co_u32_e32 v42, vcc, s18, v58
	s_mov_b32 s18, 0xf000
	s_nop 0
	v_addc_co_u32_e32 v43, vcc, 0, v59, vcc
	v_add_co_u32_e32 v46, vcc, s18, v58
	s_mov_b32 s18, 0x14000
	s_nop 0
	v_addc_co_u32_e32 v47, vcc, 0, v59, vcc
	v_add_co_u32_e32 v50, vcc, s18, v58
	s_mov_b32 s18, 0x18000
	s_nop 0
	v_addc_co_u32_e32 v51, vcc, 0, v59, vcc
	v_add_co_u32_e32 v54, vcc, s18, v58
	global_load_dwordx4 v[34:37], v[34:35], off offset:128
	s_nop 0
	global_load_dwordx4 v[38:41], v[38:39], off offset:3200
	v_addc_co_u32_e32 v55, vcc, 0, v59, vcc
	v_add_co_u32_e32 v60, vcc, 0x1d000, v58
	global_load_dwordx4 v[42:45], v[42:43], off offset:2176
	s_nop 0
	global_load_dwordx4 v[46:49], v[46:47], off offset:1152
	v_addc_co_u32_e32 v61, vcc, 0, v59, vcc
	v_add_co_u32_e32 v62, vcc, 0x22000, v58
	global_load_dwordx4 v[50:53], v[50:51], off offset:128
	s_nop 0
	global_load_dwordx4 v[54:57], v[54:55], off offset:3200
	v_addc_co_u32_e32 v63, vcc, 0, v59, vcc
	global_load_dwordx4 v[58:61], v[60:61], off offset:2176
	s_nop 0
	global_load_dwordx4 v[62:65], v[62:63], off offset:1152
	s_and_b32 s20, s88, 31
	s_ashr_i32 s18, s88, 3
	s_lshl_b32 s70, s20, 6
	s_and_b32 s89, s18, -4
	v_mbcnt_hi_u32_b32 v219, -1, v213
	s_and_saveexec_b64 s[18:19], s[4:5]
	s_cbranch_execz .LBB0_438
	v_or_b32_e32 v98, s89, v1
	v_ashrrev_i32_e32 v99, 31, v98
	v_lshlrev_b64 v[98:99], 11, v[98:99]
	v_or_b32_e32 v98, s70, v98
	v_or_b32_e32 v98, v98, v122
	v_lshlrev_b64 v[98:99], 2, v[98:99]
	v_lshl_add_u64 v[100:101], s[74:75], 0, v[98:99]
	global_load_dword v102, v[100:101], off
	v_lshl_add_u64 v[100:101], s[72:73], 0, v[98:99]
	global_load_dword v100, v[100:101], off
	v_and_b32_e32 v101, 64, v219
	v_add_u32_e32 v103, -1, v219
	v_cmp_lt_i32_e32 vcc, v103, v101
	v_add_u32_e32 v105, -2, v219
	v_add_u32_e32 v106, -4, v219
	v_cndmask_b32_e32 v103, v103, v219, vcc
	v_lshlrev_b32_e32 v103, 2, v103
	v_cmp_lt_i32_e32 vcc, v105, v101
	v_add_u32_e32 v107, -8, v219
	v_add_u32_e32 v108, -16, v219
	v_cndmask_b32_e32 v105, v105, v219, vcc
	v_lshlrev_b32_e32 v105, 2, v105
	v_cmp_lt_i32_e32 vcc, v106, v101
	v_subrev_u32_e32 v109, 32, v219
	s_waitcnt vmcnt(1)
	ds_bpermute_b32 v104, v103, v102
	v_cndmask_b32_e32 v106, v106, v219, vcc
	v_lshlrev_b32_e32 v106, 2, v106
	v_cmp_lt_i32_e32 vcc, v107, v101
	s_waitcnt lgkmcnt(0)
	v_add_f32_e32 v104, v102, v104
	v_cndmask_b32_e64 v102, v104, v102, s[6:7]
	ds_bpermute_b32 v104, v105, v102
	v_cndmask_b32_e32 v107, v107, v219, vcc
	v_lshlrev_b32_e32 v107, 2, v107
	v_cmp_lt_i32_e32 vcc, v108, v101
	s_waitcnt lgkmcnt(0)
	v_add_f32_e32 v104, v102, v104
	v_cndmask_b32_e64 v102, v104, v102, s[8:9]
	ds_bpermute_b32 v104, v106, v102
	v_cndmask_b32_e32 v108, v108, v219, vcc
	v_lshlrev_b32_e32 v108, 2, v108
	v_cmp_lt_i32_e32 vcc, v109, v101
	s_waitcnt lgkmcnt(0)
	v_add_f32_e32 v104, v102, v104
	v_cndmask_b32_e64 v102, v104, v102, s[10:11]
	ds_bpermute_b32 v104, v107, v102
	v_cndmask_b32_e32 v101, v109, v219, vcc
	v_lshlrev_b32_e32 v109, 2, v101
	s_waitcnt lgkmcnt(0)
	v_add_f32_e32 v104, v102, v104
	v_cndmask_b32_e64 v102, v104, v102, s[12:13]
	ds_bpermute_b32 v104, v108, v102
	s_waitcnt lgkmcnt(0)
	v_add_f32_e32 v101, v102, v104
	v_cndmask_b32_e64 v101, v101, v102, s[14:15]
	ds_bpermute_b32 v102, v109, v101
	s_waitcnt lgkmcnt(0)
	v_add_f32_e32 v102, v101, v102
	v_cndmask_b32_e64 v104, v102, v101, s[16:17]
	s_waitcnt vmcnt(0)
	v_sub_f32_e32 v110, v100, v104
	ds_bpermute_b32 v100, v103, v110
	s_waitcnt lgkmcnt(0)
	v_max_f32_e32 v100, v100, v100
	v_max_f32_e32 v100, v110, v100
	v_cndmask_b32_e64 v100, v100, v110, s[6:7]
	ds_bpermute_b32 v101, v105, v100
	s_waitcnt lgkmcnt(0)
	v_max_f32_e32 v101, v101, v101
	v_max_f32_e32 v101, v100, v101
	v_cndmask_b32_e64 v100, v101, v100, s[8:9]
	ds_bpermute_b32 v101, v106, v100
	s_waitcnt lgkmcnt(0)
	v_max_f32_e32 v101, v101, v101
	v_max_f32_e32 v101, v100, v101
	v_cndmask_b32_e64 v100, v101, v100, s[10:11]
	ds_bpermute_b32 v101, v107, v100
	s_waitcnt lgkmcnt(0)
	v_max_f32_e32 v101, v101, v101
	v_max_f32_e32 v101, v100, v101
	v_cndmask_b32_e64 v102, v101, v100, s[12:13]
	ds_bpermute_b32 v103, v108, v102
	v_lshl_add_u64 v[100:101], s[76:77], 0, v[98:99]
	s_waitcnt lgkmcnt(0)
	v_max_f32_e32 v103, v103, v103
	v_max_f32_e32 v103, v102, v103
	v_cndmask_b32_e64 v105, v103, v102, s[14:15]
	ds_bpermute_b32 v106, v109, v105
	v_lshl_add_u64 v[102:103], s[78:79], 0, v[98:99]
	global_store_dword v[100:101], v104, off
	global_store_dword v[102:103], v110, off
	v_max_f32_e32 v100, v105, v105
	v_lshl_add_u64 v[98:99], s[80:81], 0, v[98:99]
	s_waitcnt lgkmcnt(0)
	v_max_f32_e32 v101, v106, v106
	v_max_f32_e32 v100, v100, v101
	v_cndmask_b32_e64 v100, v100, v105, s[16:17]
	global_store_dword v[98:99], v100, off
.LBB0_438:
	s_or_b64 exec, exec, s[18:19]
	v_mov_b32_e32 v100, v0
	s_lshl_b32 s18, s20, 8
	v_lshlrev_b32_e32 v98, 3, v100
	v_lshrrev_b32_e32 v99, 7, v100
	v_and_b32_e32 v101, 56, v98
	v_lshlrev_b32_e32 v230, 1, v100
	v_and_b32_e32 v230, 0x80, v230
	v_or_b32_e32 v101, v101, v230
	v_and_or_b32 v98, v99, 3, s89
	v_ashrrev_i32_e32 v99, 31, v98
	v_lshlrev_b64 v[98:99], 13, v[98:99]
	v_or3_b32 v98, v98, s18, v101
	v_ashrrev_i32_e32 v100, 3, v100
	v_lshlrev_b64 v[98:99], 7, v[98:99]
	v_and_b32_e32 v100, 7, v100
	v_lshlrev_b32_e32 v100, 3, v100
	v_lshl_add_u64 v[98:99], s[62:63], 0, v[98:99]
	v_ashrrev_i32_e32 v101, 31, v100
	v_lshl_add_u64 v[102:103], v[100:101], 1, v[98:99]
	v_mov_b32_e32 v230, 0x2000
	v_mov_b32_e32 v231, 0
	v_lshl_add_u64 v[228:229], v[102:103], 0, v[230:231]
	s_waitcnt vmcnt(15)
	v_and_b32_e32 v98, 0xffff, v66
	s_waitcnt vmcnt(13)
	v_and_b32_e32 v99, 0xffff, v74
	s_waitcnt vmcnt(11)
	v_and_b32_e32 v100, 0xffff, v82
	s_waitcnt vmcnt(9)
	v_and_b32_e32 v101, 0xffff, v90
	v_lshl_or_b32 v98, v70, 16, v98
	v_lshl_or_b32 v99, v78, 16, v99
	v_lshl_or_b32 v100, v86, 16, v100
	s_waitcnt vmcnt(8)
	v_lshl_or_b32 v101, v94, 16, v101
	v_lshrrev_b32_e32 v66, 16, v66
	global_store_dwordx4 v[102:103], v[98:101], off
	s_mov_b64 s[18:19], 0x2000
	s_nop 0
	v_and_or_b32 v98, v70, s95, v66
	v_lshrrev_b32_e32 v66, 16, v74
	v_and_or_b32 v99, v78, s95, v66
	v_lshrrev_b32_e32 v66, 16, v82
	v_and_or_b32 v100, v86, s95, v66
	v_lshrrev_b32_e32 v66, 16, v90
	v_and_or_b32 v101, v94, s95, v66
	v_and_b32_e32 v66, 0xffff, v67
	global_store_dwordx4 v[102:103], v[98:101], off offset:128
	v_mov_b32_e32 v70, 0
	s_nop 0
	v_lshl_or_b32 v98, v71, 16, v66
	v_and_b32_e32 v66, 0xffff, v75
	v_lshl_or_b32 v99, v79, 16, v66
	v_and_b32_e32 v66, 0xffff, v83
	v_lshl_or_b32 v100, v87, 16, v66
	v_and_b32_e32 v66, 0xffff, v91
	v_lshl_or_b32 v101, v95, 16, v66
	v_lshrrev_b32_e32 v66, 16, v67
	global_store_dwordx4 v[102:103], v[98:101], off offset:256
	v_lshrrev_b32_e32 v67, 16, v77
	v_and_or_b32 v67, v81, s95, v67
	v_and_or_b32 v98, v71, s95, v66
	v_lshrrev_b32_e32 v66, 16, v75
	v_and_or_b32 v99, v79, s95, v66
	v_lshrrev_b32_e32 v66, 16, v83
	v_and_or_b32 v100, v87, s95, v66
	v_lshrrev_b32_e32 v66, 16, v91
	v_and_or_b32 v101, v95, s95, v66
	v_and_b32_e32 v66, 0xffff, v68
	global_store_dwordx4 v[102:103], v[98:101], off offset:384
	s_nop 1
	v_lshl_or_b32 v98, v72, 16, v66
	v_and_b32_e32 v66, 0xffff, v76
	v_lshl_or_b32 v99, v80, 16, v66
	v_and_b32_e32 v66, 0xffff, v84
	v_lshl_or_b32 v100, v88, 16, v66
	v_and_b32_e32 v66, 0xffff, v92
	v_lshl_or_b32 v101, v96, 16, v66
	v_lshrrev_b32_e32 v66, 16, v68
	global_store_dwordx4 v[102:103], v[98:101], off offset:512
	v_lshrrev_b32_e32 v68, 16, v85
	v_and_or_b32 v68, v89, s95, v68
	v_and_or_b32 v98, v72, s95, v66
	v_lshrrev_b32_e32 v66, 16, v76
	v_and_or_b32 v99, v80, s95, v66
	v_lshrrev_b32_e32 v66, 16, v84
	v_and_or_b32 v100, v88, s95, v66
	v_lshrrev_b32_e32 v66, 16, v92
	v_and_or_b32 v101, v96, s95, v66
	v_and_b32_e32 v66, 0xffff, v69
	global_store_dwordx4 v[102:103], v[98:101], off offset:640
	s_nop 1
	v_lshl_or_b32 v98, v73, 16, v66
	v_and_b32_e32 v66, 0xffff, v77
	v_lshl_or_b32 v99, v81, 16, v66
	v_and_b32_e32 v66, 0xffff, v85
	v_lshl_or_b32 v100, v89, 16, v66
	v_and_b32_e32 v66, 0xffff, v93
	v_lshl_or_b32 v101, v97, 16, v66
	v_lshrrev_b32_e32 v66, 16, v69
	v_lshrrev_b32_e32 v69, 16, v93
	v_and_or_b32 v66, v73, s95, v66
	v_and_or_b32 v69, v97, s95, v69
	global_store_dwordx4 v[102:103], v[66:69], off offset:896
	global_store_dwordx4 v[102:103], v[98:101], off offset:768
	s_waitcnt vmcnt(15)
	v_and_b32_e32 v66, 0xffff, v34
	s_waitcnt vmcnt(13)
	v_and_b32_e32 v67, 0xffff, v42
	s_waitcnt vmcnt(11)
	v_and_b32_e32 v68, 0xffff, v50
	s_waitcnt vmcnt(9)
	v_and_b32_e32 v69, 0xffff, v58
	v_lshl_or_b32 v66, v38, 16, v66
	v_lshl_or_b32 v67, v46, 16, v67
	v_lshl_or_b32 v68, v54, 16, v68
	s_waitcnt vmcnt(8)
	v_lshl_or_b32 v69, v62, 16, v69
	v_lshrrev_b32_e32 v34, 16, v34
	global_store_dwordx4 v[228:229], v[66:69], off
	s_nop 1
	v_and_or_b32 v66, v38, s95, v34
	v_lshrrev_b32_e32 v34, 16, v42
	v_and_or_b32 v67, v46, s95, v34
	v_lshrrev_b32_e32 v34, 16, v50
	v_and_or_b32 v68, v54, s95, v34
	v_lshrrev_b32_e32 v34, 16, v58
	v_and_or_b32 v69, v62, s95, v34
	v_and_b32_e32 v34, 0xffff, v35
	global_store_dwordx4 v[228:229], v[66:69], off offset:128
	s_nop 1
	v_lshl_or_b32 v66, v39, 16, v34
	v_and_b32_e32 v34, 0xffff, v43
	v_lshl_or_b32 v67, v47, 16, v34
	v_and_b32_e32 v34, 0xffff, v51
	v_lshl_or_b32 v68, v55, 16, v34
	v_and_b32_e32 v34, 0xffff, v59
	v_lshl_or_b32 v69, v63, 16, v34
	v_lshrrev_b32_e32 v34, 16, v35
	global_store_dwordx4 v[228:229], v[66:69], off offset:256
	v_lshrrev_b32_e32 v35, 16, v45
	v_and_or_b32 v35, v49, s95, v35
	v_and_or_b32 v66, v39, s95, v34
	v_lshrrev_b32_e32 v34, 16, v43
	v_and_or_b32 v67, v47, s95, v34
	v_lshrrev_b32_e32 v34, 16, v51
	v_and_or_b32 v68, v55, s95, v34
	v_lshrrev_b32_e32 v34, 16, v59
	v_and_or_b32 v69, v63, s95, v34
	v_and_b32_e32 v34, 0xffff, v36
	global_store_dwordx4 v[228:229], v[66:69], off offset:384
	s_nop 1
	v_lshl_or_b32 v66, v40, 16, v34
	v_and_b32_e32 v34, 0xffff, v44
	v_lshl_or_b32 v67, v48, 16, v34
	v_and_b32_e32 v34, 0xffff, v52
	v_lshl_or_b32 v68, v56, 16, v34
	v_and_b32_e32 v34, 0xffff, v60
	v_lshl_or_b32 v69, v64, 16, v34
	v_lshrrev_b32_e32 v34, 16, v36
	global_store_dwordx4 v[228:229], v[66:69], off offset:512
	v_lshrrev_b32_e32 v36, 16, v53
	v_and_or_b32 v36, v57, s95, v36
	v_and_or_b32 v66, v40, s95, v34
	v_lshrrev_b32_e32 v34, 16, v44
	v_and_or_b32 v67, v48, s95, v34
	v_lshrrev_b32_e32 v34, 16, v52
	v_and_or_b32 v68, v56, s95, v34
	v_lshrrev_b32_e32 v34, 16, v60
	v_and_or_b32 v69, v64, s95, v34
	v_and_b32_e32 v34, 0xffff, v37
	global_store_dwordx4 v[228:229], v[66:69], off offset:640
	s_nop 1
	v_lshl_or_b32 v66, v41, 16, v34
	v_and_b32_e32 v34, 0xffff, v45
	v_lshl_or_b32 v67, v49, 16, v34
	v_and_b32_e32 v34, 0xffff, v53
	v_lshl_or_b32 v68, v57, 16, v34
	v_and_b32_e32 v34, 0xffff, v61
	v_lshl_or_b32 v69, v65, 16, v34
	v_lshrrev_b32_e32 v34, 16, v37
	v_lshrrev_b32_e32 v37, 16, v61
	global_store_dwordx4 v[228:229], v[66:69], off offset:768
	v_and_or_b32 v34, v41, s95, v34
	v_and_or_b32 v37, v65, s95, v37
	v_mov_b32_e32 v66, v0
	global_store_dwordx4 v[228:229], v[34:37], off offset:896
	v_mov_b32_e32 v67, 0
	v_lshlrev_b32_e32 v83, 3, v66
	v_and_b32_e32 v82, 0x7f8, v83
	v_lshlrev_b32_e32 v126, 2, v82
	v_lshl_add_u64 v[50:51], s[84:85], 0, v[126:127]
	v_add_co_u32_e32 v42, vcc, s96, v50
	v_lshl_add_u64 v[46:47], v[50:51], 0, s[18:19]
	s_nop 0
	v_addc_co_u32_e32 v43, vcc, 0, v51, vcc
	s_mov_b64 s[18:19], 0x4000
	v_add_co_u32_e32 v54, vcc, s97, v50
	v_lshl_add_u64 v[52:53], v[50:51], 0, s[18:19]
	s_nop 0
	v_addc_co_u32_e32 v55, vcc, 0, v51, vcc
	s_mov_b64 s[18:19], 0x6000
	global_load_dwordx4 v[34:37], v126, s[84:85] offset:16
	global_load_dwordx4 v[38:41], v126, s[84:85]
	s_nop 0
	global_load_dwordx4 v[42:45], v[42:43], off
	s_nop 0
	global_load_dwordx4 v[46:49], v[46:47], off offset:16
	s_nop 0
	global_load_dwordx4 v[58:61], v[54:55], off
	global_load_dwordx4 v[62:65], v[52:53], off offset:16
	v_lshl_add_u64 v[54:55], v[50:51], 0, s[18:19]
	v_add_co_u32_e32 v50, vcc, s54, v50
	v_ashrrev_i32_e32 v66, 3, v66
	s_nop 0
	v_addc_co_u32_e32 v51, vcc, 0, v51, vcc
	global_load_dwordx4 v[50:53], v[50:51], off
	s_nop 0
	global_load_dwordx4 v[54:57], v[54:55], off offset:16
	v_and_b32_e32 v78, 0xffffffe0, v66
	s_add_u32 s18, s42, -3
	v_add_u32_e32 v75, s70, v78
	v_ashrrev_i32_e32 v79, 31, v78
	s_addc_u32 s19, s43, -1
	v_lshlrev_b32_e32 v126, 1, v82
	v_lshl_add_u64 v[80:81], s[18:19], 0, v[78:79]
	v_lshl_add_u64 v[134:135], s[60:61], 0, v[126:127]
	v_cmp_lt_i32_e32 vcc, 2, v75
	v_mov_b32_e32 v66, 0
	v_mov_b32_e32 v68, 0
	v_mov_b32_e32 v69, 0
	s_and_saveexec_b64 s[18:19], vcc
	s_cbranch_execz .LBB0_440
	v_mad_u64_u32 v[66:67], s[20:21], v80, s93, v[134:135]
	v_mad_i32_i24 v67, v81, s93, v67
	global_load_dwordx4 v[66:69], v[66:67], off
